# speedup vs baseline: 1.0006x; 1.0006x over previous
.Lmfill_a:
	v_add_f32_e32 v242, v242, v94
	s_mov_b64 s[2:3], 0
	s_branch .Lmpb_a

.Lmpb_ret_a:
	s_mov_b64 s[26:27], -1
	s_and_b64 vcc, exec, s[24:25]
	s_cbranch_vccnz .LBB3_53
	s_andn2_b64 vcc, exec, s[26:27]
	s_cbranch_vccz .LBB3_58

.Lmfill_b:
	v_add_f32_e32 v242, v242, v106
	s_mov_b64 s[28:29], 0
	s_branch .Lmpb_b

.Lmpb_ret_b:
	s_mov_b64 s[2:3], -1
	s_and_b64 vcc, exec, s[26:27]
	s_cbranch_vccnz .LBB3_59
	s_andn2_b64 vcc, exec, s[2:3]
	s_cbranch_vccz .LBB3_64

.LBB3_72:
	v_add_u32_e32 v128, s43, v227
	ds_read_b64_tr_b16 v[118:119], v128 offset:24576
	ds_read_b64_tr_b16 v[120:121], v128 offset:25088
	v_add_f32_e32 v98, v82, v83
	v_add_f32_e32 v98, v84, v98
	v_add_f32_e32 v98, v85, v98
	v_add_f32_e32 v98, v86, v98
	v_add_f32_e32 v122, v87, v98
	s_waitcnt lgkmcnt(9)
	v_mfma_f32_32x32x16_f16 v[98:113], v[190:193], v[154:157], v[50:65]
	v_cvt_pk_f16_f32 v158, v82, v83
	v_cvt_pk_f16_f32 v159, v84, v85
	ds_read_b64_tr_b16 v[114:115], v128 offset:28672
	ds_read_b64_tr_b16 v[116:117], v128 offset:29184
	s_waitcnt lgkmcnt(10)
	v_mfma_f32_32x32x16_f16 v[50:65], v[186:189], v[154:157], v[50:65]
	v_add_f32_e32 v82, v88, v122
	v_add_f32_e32 v82, v89, v82
	v_add_f32_e32 v82, v90, v82
	v_add_f32_e32 v82, v91, v82
	v_cvt_pk_f16_f32 v160, v86, v87
	v_cvt_pk_f16_f32 v161, v88, v89
	ds_read_b64_tr_b16 v[122:123], v128 offset:25600
	ds_read_b64_tr_b16 v[124:125], v128 offset:26112
	s_waitcnt lgkmcnt(11)
	v_mfma_f32_32x32x16_f16 v[98:113], v[182:185], v[146:149], v[98:113]
	v_add_f32_e32 v82, v92, v82
	v_add_f32_e32 v82, v93, v82
	v_add_f32_e32 v82, v94, v82
	v_add_f32_e32 v82, v95, v82
	v_cvt_pk_f16_f32 v150, v90, v91
	v_cvt_pk_f16_f32 v151, v92, v93
	ds_read_b64_tr_b16 v[182:183], v128 offset:29696
	ds_read_b64_tr_b16 v[184:185], v128 offset:30208
	s_waitcnt lgkmcnt(12)
	v_mfma_f32_32x32x16_f16 v[50:65], v[178:181], v[146:149], v[50:65]
	v_add_f32_e32 v82, v96, v82
	v_add_f32_e32 v82, v97, v82
	v_add_f32_e32 v82, v66, v82
	v_add_f32_e32 v82, v67, v82
	v_cvt_pk_f16_f32 v152, v94, v95
	v_cvt_pk_f16_f32 v153, v96, v97
	ds_read_b64_tr_b16 v[154:155], v128 offset:26624
	ds_read_b64_tr_b16 v[156:157], v128 offset:27136
	s_waitcnt lgkmcnt(13)
	v_mfma_f32_32x32x16_f16 v[98:113], v[174:177], v[138:141], v[98:113]
	v_add_f32_e32 v82, v68, v82
	v_add_f32_e32 v82, v69, v82
	v_add_f32_e32 v82, v70, v82
	v_add_f32_e32 v82, v71, v82
	v_cvt_pk_f16_f32 v142, v66, v67
	v_cvt_pk_f16_f32 v143, v68, v69
	ds_read_b64_tr_b16 v[146:147], v128 offset:30720
	ds_read_b64_tr_b16 v[148:149], v128 offset:31232
	s_waitcnt lgkmcnt(14)
	v_mfma_f32_32x32x16_f16 v[50:65], v[170:173], v[138:141], v[50:65]
	v_add_f32_e32 v66, v72, v82
	v_add_f32_e32 v66, v73, v66
	v_add_f32_e32 v66, v74, v66
	v_add_f32_e32 v66, v75, v66
	v_cvt_pk_f16_f32 v144, v70, v71
	v_cvt_pk_f16_f32 v145, v72, v73
	ds_read_b64_tr_b16 v[138:139], v128 offset:27648
	ds_read_b64_tr_b16 v[140:141], v128 offset:28160
	s_waitcnt lgkmcnt(14)
	v_mfma_f32_32x32x16_f16 v[98:113], v[166:169], v[130:133], v[98:113]
	v_add_f32_e32 v66, v76, v66
	v_add_f32_e32 v66, v77, v66
	v_add_f32_e32 v66, v78, v66
	v_add_f32_e32 v66, v79, v66
	v_cvt_pk_f16_f32 v134, v74, v75
	v_cvt_pk_f16_f32 v135, v76, v77
	ds_read_b64_tr_b16 v[126:127], v128 offset:31744
	ds_read_b64_tr_b16 v[128:129], v128 offset:32256
	v_mfma_f32_32x32x16_f16 v[50:65], v[162:165], v[130:133], v[50:65]
	v_add_f32_e32 v66, v80, v66
	v_add_f32_e32 v66, v81, v66
	v_add_f32_e32 v82, 0, v66
	v_cvt_pk_f16_f32 v136, v78, v79
	v_cvt_pk_f16_f32 v137, v80, v81
	s_cmp_lt_u32 s35, 6
	s_cbranch_scc0 .Lmpart_c
	v_add_f32_e32 v98, v242, v82
	s_mov_b64 s[2:3], 0
	s_branch .Lmpb_c

.Lmpb_ret_c:
	s_andn2_b64 vcc, exec, s[2:3]
	v_lshl_add_u32 v82, v228, 2, s38
	s_cbranch_vccnz .LBB3_75
	s_waitcnt lgkmcnt(0)
	ds_read_b128 v[84:87], v82 offset:49248
	ds_read_b128 v[88:91], v82 offset:49216
	ds_read_b128 v[92:95], v82 offset:49184
	ds_read_b128 v[100:103], v82 offset:49152
	s_waitcnt lgkmcnt(3)
	v_pk_mul_f32 v[48:49], v[48:49], v[86:87]
	s_waitcnt lgkmcnt(2)
	v_pk_mul_f32 v[44:45], v[44:45], v[90:91]
	s_waitcnt lgkmcnt(1)
	v_pk_mul_f32 v[40:41], v[40:41], v[94:95]
	s_waitcnt lgkmcnt(0)
	v_pk_mul_f32 v[36:37], v[36:37], v[102:103]
	v_pk_mul_f32 v[46:47], v[46:47], v[84:85]
	v_pk_mul_f32 v[42:43], v[42:43], v[88:89]
	v_pk_mul_f32 v[38:39], v[38:39], v[92:93]
	v_pk_mul_f32 v[34:35], v[34:35], v[100:101]
	v_pk_mul_f32 v[32:33], v[32:33], v[86:87]
	v_pk_mul_f32 v[28:29], v[28:29], v[90:91]
	v_pk_mul_f32 v[24:25], v[24:25], v[94:95]
	v_pk_mul_f32 v[20:21], v[20:21], v[102:103]
	v_pk_mul_f32 v[30:31], v[30:31], v[84:85]
	v_pk_mul_f32 v[26:27], v[26:27], v[88:89]
	v_pk_mul_f32 v[22:23], v[22:23], v[92:93]
	v_pk_mul_f32 v[18:19], v[18:19], v[100:101]

.Lmpb_c:
	s_waitcnt lgkmcnt(14)
	v_mfma_f32_32x32x16_f16 v[34:49], v[158:161], v[118:121], v[34:49]
	v_mov_b32_e32 v66, 0
	v_mov_b32_e32 v67, 0
	v_mov_b32_e32 v68, 0
	v_mov_b32_e32 v69, 0
	s_waitcnt lgkmcnt(12)
	v_mfma_f32_32x32x16_f16 v[18:33], v[158:161], v[114:117], v[18:33]
	v_mov_b32_e32 v70, 0
	v_mov_b32_e32 v71, 0
	v_mov_b32_e32 v72, 0
	v_mov_b32_e32 v73, 0
	s_waitcnt lgkmcnt(10)
	v_mfma_f32_32x32x16_f16 v[34:49], v[150:153], v[122:125], v[34:49]
	v_mov_b32_e32 v74, 0
	v_mov_b32_e32 v75, 0
	v_mov_b32_e32 v76, 0
	v_mov_b32_e32 v77, 0
	s_waitcnt lgkmcnt(8)
	v_mfma_f32_32x32x16_f16 v[18:33], v[150:153], v[182:185], v[18:33]
	v_mov_b32_e32 v78, 0
	v_mov_b32_e32 v79, 0
	v_mov_b32_e32 v80, 0
	v_mov_b32_e32 v81, 0
	s_waitcnt lgkmcnt(6)
	v_mfma_f32_32x32x16_f16 v[34:49], v[142:145], v[154:157], v[34:49]
	v_mov_b32_e32 v50, 0
	v_mov_b32_e32 v51, 0
	v_mov_b32_e32 v52, 0
	v_mov_b32_e32 v53, 0
	s_waitcnt lgkmcnt(4)
	v_mfma_f32_32x32x16_f16 v[18:33], v[142:145], v[146:149], v[18:33]
	v_mov_b32_e32 v54, 0
	v_mov_b32_e32 v55, 0
	v_mov_b32_e32 v56, 0
	v_mov_b32_e32 v57, 0
	s_waitcnt lgkmcnt(2)
	v_mfma_f32_32x32x16_f16 v[34:49], v[134:137], v[138:141], v[34:49]
	v_mov_b32_e32 v58, 0
	v_mov_b32_e32 v59, 0
	v_mov_b32_e32 v60, 0
	v_mov_b32_e32 v61, 0
	s_waitcnt lgkmcnt(0)
	v_mfma_f32_32x32x16_f16 v[18:33], v[134:137], v[126:129], v[18:33]
	v_mov_b32_e32 v62, 0
	v_mov_b32_e32 v63, 0
	v_mov_b32_e32 v64, 0
	v_mov_b32_e32 v65, 0
	s_branch .Lmpb_ret_c
.Lmpb_b:
	s_waitcnt lgkmcnt(14)
	v_mfma_f32_32x32x16_f16 v[34:49], v[158:161], v[202:205], v[34:49]
	v_mov_b32_e32 v82, 0
	v_mov_b32_e32 v83, 0
	v_mov_b32_e32 v84, 0
	v_mov_b32_e32 v85, 0
	s_waitcnt lgkmcnt(12)
	v_mfma_f32_32x32x16_f16 v[18:33], v[158:161], v[198:201], v[18:33]
	v_mov_b32_e32 v86, 0
	v_mov_b32_e32 v87, 0
	v_mov_b32_e32 v88, 0
	v_mov_b32_e32 v89, 0
	v_cndmask_b32_e64 v106, 0, 1, s[30:31]
	v_cmp_ne_u32_e64 s[2:3], 1, v106
	s_andn2_b64 vcc, exec, s[30:31]
	v_add_u32_e32 v106, s42, v226
	s_cbranch_vccnz .Lmpb_b_l41
	ds_read_b128 v[190:193], v106
	ds_read_b128 v[186:189], v106 offset:512
.Lmpb_b_l41:
	s_waitcnt lgkmcnt(10)
	v_mfma_f32_32x32x16_f16 v[34:49], v[150:153], v[194:197], v[34:49]
	v_mov_b32_e32 v90, 0
	v_mov_b32_e32 v91, 0
	v_mov_b32_e32 v92, 0
	v_mov_b32_e32 v93, 0
	s_and_b64 vcc, exec, s[2:3]
	s_cbranch_vccnz .Lmpb_b_l43
	ds_read_b128 v[182:185], v106 offset:2048
	ds_read_b128 v[178:181], v106 offset:2560
.Lmpb_b_l43:
	s_waitcnt lgkmcnt(8)
	v_mfma_f32_32x32x16_f16 v[18:33], v[150:153], v[122:125], v[18:33]
	v_mov_b32_e32 v94, 0
	v_mov_b32_e32 v95, 0
	v_mov_b32_e32 v96, 0
	v_mov_b32_e32 v97, 0
	s_and_b64 vcc, exec, s[2:3]
	s_cbranch_vccnz .Lmpb_b_l45
	ds_read_b128 v[174:177], v106 offset:4096
	ds_read_b128 v[170:173], v106 offset:4608
.Lmpb_b_l45:
	s_waitcnt lgkmcnt(6)
	v_mfma_f32_32x32x16_f16 v[34:49], v[142:145], v[118:121], v[34:49]
	v_mov_b32_e32 v66, 0
	v_mov_b32_e32 v67, 0
	v_mov_b32_e32 v68, 0
	v_mov_b32_e32 v69, 0
	s_and_b64 vcc, exec, s[2:3]
	s_cbranch_vccnz .Lmpb_b_l47
	ds_read_b128 v[166:169], v106 offset:6144
	ds_read_b128 v[162:165], v106 offset:6656
.Lmpb_b_l47:
	s_waitcnt lgkmcnt(4)
	v_mfma_f32_32x32x16_f16 v[18:33], v[142:145], v[114:117], v[18:33]
	v_mov_b32_e32 v70, 0
	v_mov_b32_e32 v71, 0
	v_mov_b32_e32 v72, 0
	v_mov_b32_e32 v73, 0
	s_waitcnt lgkmcnt(2)
	v_mfma_f32_32x32x16_f16 v[34:49], v[134:137], v[102:105], v[34:49]
	v_mov_b32_e32 v74, 0
	v_mov_b32_e32 v75, 0
	v_mov_b32_e32 v76, 0
	v_mov_b32_e32 v77, 0
	s_waitcnt lgkmcnt(0)
	v_mfma_f32_32x32x16_f16 v[18:33], v[134:137], v[98:101], v[18:33]
	v_mov_b32_e32 v78, 0
	v_mov_b32_e32 v79, 0
	v_mov_b32_e32 v80, 0
	v_mov_b32_e32 v81, 0
	s_branch .Lmpb_ret_b
.Lmpb_a:
	s_waitcnt lgkmcnt(14)
	v_mfma_f32_32x32x16_f16 v[34:49], v[158:161], v[194:197], v[34:49]
	v_mov_b32_e32 v114, 0
	v_mov_b32_e32 v115, 0
	v_mov_b32_e32 v116, 0
	v_mov_b32_e32 v117, 0
	s_waitcnt lgkmcnt(12)
	v_mfma_f32_32x32x16_f16 v[18:33], v[158:161], v[190:193], v[18:33]
	v_mov_b32_e32 v118, 0
	v_mov_b32_e32 v119, 0
	v_mov_b32_e32 v120, 0
	v_mov_b32_e32 v121, 0
	v_add_u32_e32 v78, s43, v226
	ds_read_b128 v[190:193], v78
	ds_read_b128 v[186:189], v78 offset:512
	s_waitcnt lgkmcnt(12)
	v_mfma_f32_32x32x16_f16 v[34:49], v[150:153], v[82:85], v[34:49]
	v_mov_b32_e32 v122, 0
	v_mov_b32_e32 v123, 0
	v_mov_b32_e32 v124, 0
	v_mov_b32_e32 v125, 0
	ds_read_b128 v[182:185], v78 offset:2048
	ds_read_b128 v[178:181], v78 offset:2560
	s_waitcnt lgkmcnt(12)
	v_mfma_f32_32x32x16_f16 v[18:33], v[150:153], v[86:89], v[18:33]
	v_mov_b32_e32 v126, 0
	v_mov_b32_e32 v127, 0
	v_mov_b32_e32 v128, 0
	v_mov_b32_e32 v129, 0
	ds_read_b128 v[174:177], v78 offset:4096
	ds_read_b128 v[170:173], v78 offset:4608
	s_waitcnt lgkmcnt(12)
	v_mfma_f32_32x32x16_f16 v[34:49], v[142:145], v[90:93], v[34:49]
	v_mov_b32_e32 v98, 0
	v_mov_b32_e32 v99, 0
	v_mov_b32_e32 v100, 0
	v_mov_b32_e32 v101, 0
	ds_read_b128 v[166:169], v78 offset:6144
	ds_read_b128 v[162:165], v78 offset:6656
	s_waitcnt lgkmcnt(12)
	v_mfma_f32_32x32x16_f16 v[18:33], v[142:145], v[66:69], v[18:33]
	v_mov_b32_e32 v102, 0
	v_mov_b32_e32 v103, 0
	v_mov_b32_e32 v104, 0
	v_mov_b32_e32 v105, 0
	s_waitcnt lgkmcnt(10)
	v_mfma_f32_32x32x16_f16 v[34:49], v[134:137], v[70:73], v[34:49]
	v_mov_b32_e32 v106, 0
	v_mov_b32_e32 v107, 0
	v_mov_b32_e32 v108, 0
	v_mov_b32_e32 v109, 0
	s_waitcnt lgkmcnt(8)
	v_mfma_f32_32x32x16_f16 v[18:33], v[134:137], v[74:77], v[18:33]
	v_mov_b32_e32 v110, 0
	v_mov_b32_e32 v111, 0
	v_mov_b32_e32 v112, 0
	v_mov_b32_e32 v113, 0
	s_branch .Lmpb_ret_a
